# P5 m3 unit: un-normalised h rows parked in LDS (the V tile's region, free once V fragments are in registers) instead of a global-memory round trip between stage 2 and the rescale pass
# speedup vs baseline: 1.0176x; 1.0025x over previous
.LBB0_786:
	s_or_b64 exec, exec, s[60:61]
	s_waitcnt lgkmcnt(0)
	v_and_b32_sdwa v1, v33, v198 dst_sel:DWORD dst_unused:UNUSED_PAD src0_sel:WORD_1 src1_sel:DWORD
	v_add3_u32 v2, v33, v1, s71
	v_and_b32_sdwa v1, v34, v198 dst_sel:DWORD dst_unused:UNUSED_PAD src0_sel:WORD_1 src1_sel:DWORD
	v_and_b32_sdwa v3, v35, v198 dst_sel:DWORD dst_unused:UNUSED_PAD src0_sel:WORD_1 src1_sel:DWORD
	v_and_b32_sdwa v0, v32, v198 dst_sel:DWORD dst_unused:UNUSED_PAD src0_sel:WORD_1 src1_sel:DWORD
	v_add3_u32 v1, v34, v1, s71
	v_add3_u32 v3, v35, v3, s71
	v_mov_b32_e32 v147, s55
	v_or_b32_e32 v146, s54, v86
	v_add3_u32 v0, v32, v0, s71
	v_and_b32_e32 v1, 0xffff0000, v1
	v_and_b32_e32 v3, 0xffff0000, v3
	v_lshlrev_b64 v[32:33], 10, v[146:147]
	v_or_b32_sdwa v1, v1, v0 dst_sel:DWORD dst_unused:UNUSED_PAD src0_sel:DWORD src1_sel:WORD_1
	v_or_b32_sdwa v0, v3, v2 dst_sel:DWORD dst_unused:UNUSED_PAD src0_sel:DWORD src1_sel:WORD_1
	s_lshl_b64 s[60:61], s[52:53], 16
	v_lshl_add_u64 v[32:33], s[0:1], 0, v[32:33]
	s_barrier
	ds_write2_b64 v164, v[0:1], v[22:23] offset1:4
	ds_write2_b64 v164, v[20:21], v[26:27] offset0:8 offset1:12
	ds_write2_b64 v164, v[24:25], v[30:31] offset0:16 offset1:20
	ds_write2_b64 v164, v[28:29], v[16:17] offset0:24 offset1:28
	v_lshl_add_u64 v[16:17], v[120:121], 0, s[60:61]
	v_lshl_add_u64 v[32:33], v[32:33], 0, s[96:97]
	v_mov_b32_e32 v141, v85
	v_lshl_add_u64 v[12:13], v[16:17], 0, v[122:123]
	v_lshl_add_u64 v[28:29], v[16:17], 0, v[124:125]
	v_lshl_add_u64 v[32:33], v[32:33], 0, v[140:141]
	s_waitcnt lgkmcnt(0)
	s_barrier
	global_load_dwordx4 v[0:3], v[12:13], off
	global_load_dwordx4 v[4:7], v[12:13], off offset:64
	global_load_dwordx4 v[8:11], v[12:13], off offset:128
	s_nop 0
	global_load_dwordx4 v[12:15], v[12:13], off offset:192
	s_nop 0
	global_load_dwordx4 v[16:19], v[28:29], off
	global_load_dwordx4 v[20:23], v[28:29], off offset:64
	global_load_dwordx4 v[24:27], v[28:29], off offset:128
	s_nop 0
	global_load_dwordx4 v[28:31], v[28:29], off offset:192
	s_nop 0
	global_load_dwordx4 v[68:71], v[32:33], off
	global_load_dwordx4 v[60:63], v[32:33], off offset:64
	global_load_dwordx4 v[72:75], v[32:33], off offset:128
	global_load_dwordx4 v[76:79], v[32:33], off offset:192
	ds_read_b64_tr_b16 v[34:35], v165 offset:36992
	ds_read_b64_tr_b16 v[32:33], v165 offset:34816
	ds_read_b64_tr_b16 v[38:39], v165 offset:37024
	ds_read_b64_tr_b16 v[36:37], v165 offset:34848
	ds_read_b64_tr_b16 v[40:41], v166 offset:34816
	ds_read_b64_tr_b16 v[42:43], v166 offset:36992
	ds_read_b64_tr_b16 v[44:45], v166 offset:52224
	ds_read_b64_tr_b16 v[46:47], v166 offset:54400
	ds_read_b64_tr_b16 v[48:49], v165 offset:52224
	ds_read_b64_tr_b16 v[50:51], v165 offset:54400
	ds_read_b64_tr_b16 v[54:55], v165 offset:54432
	ds_read_b64_tr_b16 v[52:53], v165 offset:52256
	ds_read_b64_tr_b16 v[56:57], v167 offset:34816
	ds_read_b64_tr_b16 v[58:59], v167 offset:36992
	ds_read_b64_tr_b16 v[64:65], v167 offset:52224
	ds_read_b64_tr_b16 v[66:67], v167 offset:54400
	s_and_b32 s53, s63, 0x1f80
	s_add_u32 s58, s53, s58
	s_addc_u32 s59, 0, s59
	v_lshl_add_u64 v[80:81], s[58:59], 0, v[86:87]
	s_lshl_b32 s53, s52, 3
	v_lshlrev_b64 v[144:145], 11, v[80:81]
	s_and_b32 s53, s53, 0x600
	v_or_b32_e32 v144, s53, v144
	s_mov_b32 s49, 16
	v_lshl_add_u64 v[148:149], v[126:127], 0, s[96:97]
	v_lshl_add_u64 v[150:151], v[132:133], 0, v[144:145]
	s_mov_b64 s[58:59], 0
	v_mov_b32_e32 v84, v180
	v_mov_b32_e32 v137, v179
	v_mov_b32_e32 v139, v178
	v_mbcnt_lo_u32_b32 v240, -1, 0
	v_mbcnt_hi_u32_b32 v240, -1, v240
	v_lshlrev_b32_e32 v240, 3, v240
	v_readlane_b32 s32, v252, 1
	s_lshl_b32 s32, s32, 13
	v_add_u32_e32 v240, s32, v240
	v_add_u32_e32 v240, 0x8800, v240
	s_waitcnt lgkmcnt(0)
	s_barrier
	s_branch .LBB0_788
.LBB0_787:
	s_or_b64 exec, exec, s[60:61]
	s_add_u32 s58, s58, 0x8000
	s_addc_u32 s59, s59, 0
	s_add_i32 s49, s49, 16
	s_waitcnt vmcnt(0) lgkmcnt(0)
	v_mov_b64_e32 v[76:77], v[80:81]
	v_add_u32_e32 v139, 0x200, v139
	v_add_u32_e32 v137, 64, v137
	v_add_u32_e32 v84, 0x1100, v84
	s_cmp_eq_u32 s58, 0x40000
	v_mov_b64_e32 v[78:79], v[82:83]
	s_cbranch_scc1 .LBB0_790
.LBB0_788:
	v_add_u32_e32 v141, 0, v84
	ds_read_b128 v[200:203], v141
	ds_read_b128 v[204:207], v141 offset:64
	s_waitcnt vmcnt(3)
	v_mov_b64_e32 v[210:211], v[70:71]
	v_mov_b64_e32 v[208:209], v[68:69]
	s_waitcnt vmcnt(2)
	v_mov_b64_e32 v[218:219], v[62:63]
	s_waitcnt lgkmcnt(1)
	v_mfma_f32_16x16x32_bf16 v[80:83], v[32:35], v[200:203], 0
	s_waitcnt vmcnt(1)
	v_mov_b64_e32 v[214:215], v[74:75]
	v_mov_b64_e32 v[216:217], v[60:61]
	s_cmp_lg_u32 s58, 0x38000
	v_mfma_f32_16x16x32_bf16 v[68:71], v[0:3], v[208:211], 0
	ds_read_b128 v[220:223], v141 offset:128
	ds_read_b128 v[224:227], v141 offset:192
	v_mov_b64_e32 v[212:213], v[72:73]
	s_waitcnt lgkmcnt(2)
	v_mfma_f32_16x16x32_bf16 v[60:63], v[48:51], v[204:207], v[80:83]
	s_cselect_b32 s96, s49, 0x70
	v_add_u32_e32 v141, 0, v137
	v_add_u32_e32 v143, 0x19c00, v141
	v_mfma_f32_16x16x32_bf16 v[72:75], v[4:7], v[216:219], v[68:71]
	v_add_u32_e32 v141, 0x19e00, v141
	s_nop 1
	v_lshl_add_u64 v[68:69], v[146:147], 0, s[96:97]
	v_lshlrev_b64 v[68:69], 10, v[68:69]
	v_lshl_add_u64 v[80:81], v[148:149], 0, v[68:69]
	s_waitcnt lgkmcnt(1)
	v_mfma_f32_16x16x32_bf16 v[228:231], v[40:43], v[220:223], v[60:63]
	global_load_dwordx4 v[68:71], v[80:81], off
	s_nop 1
	global_load_dwordx4 v[60:63], v[80:81], off offset:64
	v_mfma_f32_16x16x32_bf16 v[232:235], v[8:11], v[212:215], v[72:75]
	s_nop 2
	global_load_dwordx4 v[72:75], v[80:81], off offset:128
	s_nop 0
	global_load_dwordx4 v[80:83], v[80:81], off offset:192
	ds_read_b32 v236, v143
	ds_read_b32 v238, v141
	v_mfma_f32_16x16x32_bf16 v[200:203], v[36:39], v[200:203], 0
	v_mfma_f32_16x16x32_bf16 v[208:211], v[16:19], v[208:211], 0
	v_mfma_f32_16x16x32_bf16 v[200:203], v[52:55], v[204:207], v[200:203]
	v_mfma_f32_16x16x32_bf16 v[204:207], v[20:23], v[216:219], v[208:211]
	s_waitcnt lgkmcnt(2)
	v_mfma_f32_16x16x32_bf16 v[228:231], v[44:47], v[224:227], v[228:231]
	s_waitcnt vmcnt(4)
	v_mfma_f32_16x16x32_bf16 v[232:235], v[12:15], v[76:79], v[232:235]
	v_mfma_f32_16x16x32_bf16 v[200:203], v[56:59], v[220:223], v[200:203]
	v_mfma_f32_16x16x32_bf16 v[204:207], v[24:27], v[212:215], v[204:207]
	s_waitcnt lgkmcnt(1)
	s_nop 4
	v_pk_fma_f32 v[230:231], v[236:237], v[234:235], v[230:231] op_sel_hi:[0,1,1]
	v_pk_fma_f32 v[228:229], v[236:237], v[232:233], v[228:229] op_sel_hi:[0,1,1]
	s_waitcnt lgkmcnt(0)
	v_pk_mul_f32 v[230:231], v[238:239], v[230:231] op_sel_hi:[0,1]
	v_mfma_f32_16x16x32_bf16 v[200:203], v[64:67], v[224:227], v[200:203]
	v_mul_f32_e64 v228, v238, v228
	v_mul_f32_e64 v229, v238, v229
	v_mul_f32_e32 v141, v229, v229
	v_mul_f32_e32 v143, v231, v231
	v_mfma_f32_16x16x32_bf16 v[76:79], v[28:31], v[76:79], v[204:207]
	v_fmac_f32_e32 v141, v228, v228
	v_fmac_f32_e32 v143, v230, v230
	v_and_b32_sdwa v208, v231, v198 dst_sel:DWORD dst_unused:UNUSED_PAD src0_sel:WORD_1 src1_sel:DWORD
	v_and_b32_sdwa v209, v229, v198 dst_sel:DWORD dst_unused:UNUSED_PAD src0_sel:WORD_1 src1_sel:DWORD
	v_add_f32_e32 v141, v141, v143
	v_and_b32_sdwa v143, v230, v198 dst_sel:DWORD dst_unused:UNUSED_PAD src0_sel:WORD_1 src1_sel:DWORD
	v_and_b32_sdwa v199, v228, v198 dst_sel:DWORD dst_unused:UNUSED_PAD src0_sel:WORD_1 src1_sel:DWORD
	v_add3_u32 v208, v231, v208, s71
	v_add3_u32 v209, v229, v209, s71
	v_pk_fma_f32 v[78:79], v[236:237], v[78:79], v[202:203] op_sel_hi:[0,1,1]
	v_pk_fma_f32 v[76:77], v[236:237], v[76:77], v[200:201] op_sel_hi:[0,1,1]
	v_add3_u32 v199, v228, v199, s71
	v_add3_u32 v143, v230, v143, s71
	v_and_b32_e32 v208, 0xffff0000, v208
	v_and_b32_e32 v210, 0xffff0000, v209
	v_pk_mul_f32 v[78:79], v[238:239], v[78:79] op_sel_hi:[0,1]
	v_pk_mul_f32 v[76:77], v[238:239], v[76:77] op_sel_hi:[0,1]
	v_or_b32_sdwa v209, v208, v143 dst_sel:DWORD dst_unused:UNUSED_PAD src0_sel:DWORD src1_sel:WORD_1
	v_or_b32_sdwa v208, v210, v199 dst_sel:DWORD dst_unused:UNUSED_PAD src0_sel:DWORD src1_sel:WORD_1
	v_mul_f32_e32 v143, v77, v77
	v_mul_f32_e32 v199, v79, v79
	v_fmac_f32_e32 v143, v76, v76
	v_fmac_f32_e32 v199, v78, v78
	v_add_f32_e32 v143, v143, v199
	v_add_f32_e32 v141, v141, v143
	v_and_b32_sdwa v143, v78, v198 dst_sel:DWORD dst_unused:UNUSED_PAD src0_sel:WORD_1 src1_sel:DWORD
	v_add3_u32 v78, v78, v143, s71
	ds_bpermute_b32 v143, v160, v141
	v_and_b32_sdwa v199, v76, v198 dst_sel:DWORD dst_unused:UNUSED_PAD src0_sel:WORD_1 src1_sel:DWORD
	v_add3_u32 v199, v76, v199, s71
	v_and_b32_sdwa v76, v79, v198 dst_sel:DWORD dst_unused:UNUSED_PAD src0_sel:WORD_1 src1_sel:DWORD
	v_and_b32_sdwa v200, v77, v198 dst_sel:DWORD dst_unused:UNUSED_PAD src0_sel:WORD_1 src1_sel:DWORD
	v_add3_u32 v76, v79, v76, s71
	v_add3_u32 v79, v77, v200, s71
	v_and_b32_e32 v200, 0xffff0000, v76
	s_waitcnt lgkmcnt(0)
	v_add_f32_e32 v76, v141, v143
	ds_bpermute_b32 v77, v161, v76
	v_lshl_add_u64 v[210:211], v[150:151], 0, s[58:59]
	v_add_co_u32_e32 v210, vcc, s72, v210
	v_and_b32_e32 v141, 0xffff0000, v79
	s_nop 0
	v_addc_co_u32_e32 v211, vcc, 0, v211, vcc
	v_or_b32_sdwa v79, v200, v78 dst_sel:DWORD dst_unused:UNUSED_PAD src0_sel:DWORD src1_sel:WORD_1
	v_or_b32_sdwa v78, v141, v199 dst_sel:DWORD dst_unused:UNUSED_PAD src0_sel:DWORD src1_sel:WORD_1
	s_lshr_b32 s32, s58, 5
	v_add_u32_e32 v241, s32, v240
	ds_write_b64 v241, v[208:209]
	ds_write_b64 v241, v[78:79] offset:512
	s_and_saveexec_b64 s[60:61], s[10:11]
	s_cbranch_execz .LBB0_787
	v_add_u32_e32 v78, 0, v139
	s_waitcnt lgkmcnt(0)
	v_add_f32_e32 v76, v76, v77
	ds_write_b32 v78, v76
	s_branch .LBB0_787
.LBB0_790:
	s_lshl_b32 s96, s56, 1
	s_add_u32 s58, s42, s96
	s_addc_u32 s59, s43, 0
	v_mov_b32_e32 v143, v85
	v_mov_b64_e32 v[0:1], s[88:89]
	v_lshl_add_u64 v[10:11], s[58:59], 0, v[142:143]
	v_mad_u64_u32 v[0:1], s[58:59], v146, s65, v[0:1]
	v_mov_b32_e32 v2, v1
	v_mad_u64_u32 v[2:3], s[58:59], v147, s65, v[2:3]
	v_mov_b32_e32 v1, v2
	v_lshl_add_u64 v[0:1], v[0:1], 0, s[96:97]
	v_lshl_add_u64 v[0:1], v[0:1], 0, v[142:143]
	s_mov_b32 s49, s97
	v_lshl_add_u64 v[0:1], v[0:1], 0, s[48:49]
	v_lshl_add_u64 v[2:3], v[0:1], 0, s[50:51]
	v_add_co_u32_e32 v0, vcc, s73, v0
	s_lshl_b32 s56, s56, 2
	s_nop 0
	v_addc_co_u32_e32 v1, vcc, 0, v1, vcc
	global_load_dwordx2 v[22:23], v[0:1], off offset:2560
	global_load_dwordx2 v[16:17], v[2:3], off offset:32
	v_lshlrev_b64 v[0:1], 11, v[146:147]
	v_lshl_add_u64 v[0:1], s[42:43], 0, v[0:1]
	v_lshl_add_u64 v[0:1], v[0:1], 0, s[96:97]
	s_mov_b32 s57, s97
	v_lshl_add_u64 v[4:5], v[0:1], 0, v[142:143]
	v_lshl_add_u64 v[6:7], v[130:131], 0, s[56:57]
	global_load_dwordx4 v[0:3], v[6:7], off
	v_lshl_add_u64 v[8:9], v[4:5], 0, s[48:49]
	ds_read_b64 v[26:27], v240
	s_nop 0
	global_load_dwordx4 v[4:7], v[6:7], off offset:64
	s_nop 0
	ds_read_b64 v[24:25], v240 offset:512
	s_mov_b64 s[56:57], 0
	s_mov_b32 s53, 16
	v_mov_b32_e32 v29, v181
	v_lshl_add_u64 v[32:33], v[10:11], 0, s[48:49]
	s_movk_i32 s58, 0x10
	v_or_b32_e32 v84, s58, v86
	v_lshl_add_u64 v[12:13], s[54:55], 0, v[84:85]
	v_mov_b64_e32 v[14:15], s[88:89]
	v_mad_u64_u32 v[14:15], s[58:59], v12, s65, v[14:15]
	v_mov_b32_e32 v18, v15
	v_mad_u64_u32 v[18:19], s[58:59], v13, s65, v[18:19]
	v_mov_b32_e32 v15, v18
	v_lshl_add_u64 v[14:15], v[14:15], 0, s[96:97]
	v_lshl_add_u64 v[14:15], v[14:15], 0, v[142:143]
	v_lshl_add_u64 v[14:15], v[14:15], 0, s[48:49]
	v_lshl_add_u64 v[20:21], v[14:15], 0, s[50:51]
	v_add_co_u32_e32 v14, vcc, s73, v14
	v_lshlrev_b64 v[12:13], 11, v[12:13]
	s_nop 0
	v_addc_co_u32_e32 v15, vcc, 0, v15, vcc
	global_load_dwordx2 v[40:41], v[14:15], off offset:2560
	v_lshl_add_u64 v[14:15], v[32:33], 0, v[12:13]
	ds_read_b64 v[42:43], v240 offset:1024
	s_nop 0
	global_load_dwordx2 v[44:45], v[20:21], off offset:32
	s_nop 0
	ds_read_b64 v[46:47], v240 offset:1536
	s_movk_i32 s58, 0x20
	v_or_b32_e32 v84, s58, v86
	v_lshl_add_u64 v[12:13], s[54:55], 0, v[84:85]
	v_mov_b64_e32 v[14:15], s[88:89]
	v_mad_u64_u32 v[14:15], s[58:59], v12, s65, v[14:15]
	v_mov_b32_e32 v18, v15
	v_mad_u64_u32 v[18:19], s[58:59], v13, s65, v[18:19]
	v_mov_b32_e32 v15, v18
	v_lshl_add_u64 v[14:15], v[14:15], 0, s[96:97]
	v_lshl_add_u64 v[14:15], v[14:15], 0, v[142:143]
	v_lshl_add_u64 v[14:15], v[14:15], 0, s[48:49]
	v_lshl_add_u64 v[20:21], v[14:15], 0, s[50:51]
	v_add_co_u32_e32 v14, vcc, s73, v14
	v_lshlrev_b64 v[12:13], 11, v[12:13]
	s_nop 0
	v_addc_co_u32_e32 v15, vcc, 0, v15, vcc
	global_load_dwordx2 v[48:49], v[14:15], off offset:2560
	v_lshl_add_u64 v[14:15], v[32:33], 0, v[12:13]
	ds_read_b64 v[50:51], v240 offset:2048
	s_nop 0
	global_load_dwordx2 v[52:53], v[20:21], off offset:32
	s_nop 0
	ds_read_b64 v[54:55], v240 offset:2560
	s_movk_i32 s58, 0x30
	v_or_b32_e32 v84, s58, v86
	v_lshl_add_u64 v[12:13], s[54:55], 0, v[84:85]
	v_mov_b64_e32 v[14:15], s[88:89]
	v_mad_u64_u32 v[14:15], s[58:59], v12, s65, v[14:15]
	v_mov_b32_e32 v18, v15
	v_mad_u64_u32 v[18:19], s[58:59], v13, s65, v[18:19]
	v_mov_b32_e32 v15, v18
	v_lshl_add_u64 v[14:15], v[14:15], 0, s[96:97]
	v_lshl_add_u64 v[14:15], v[14:15], 0, v[142:143]
	v_lshl_add_u64 v[14:15], v[14:15], 0, s[48:49]
	v_lshl_add_u64 v[20:21], v[14:15], 0, s[50:51]
	v_add_co_u32_e32 v14, vcc, s73, v14
	v_lshlrev_b64 v[12:13], 11, v[12:13]
	s_nop 0
	v_addc_co_u32_e32 v15, vcc, 0, v15, vcc
	global_load_dwordx2 v[56:57], v[14:15], off offset:2560
	v_lshl_add_u64 v[14:15], v[32:33], 0, v[12:13]
	ds_read_b64 v[58:59], v240 offset:3072
	s_nop 0
	global_load_dwordx2 v[60:61], v[20:21], off offset:32
	s_nop 0
	ds_read_b64 v[62:63], v240 offset:3584
	s_movk_i32 s58, 0x40
	v_or_b32_e32 v84, s58, v86
	v_lshl_add_u64 v[12:13], s[54:55], 0, v[84:85]
	v_mov_b64_e32 v[14:15], s[88:89]
	v_mad_u64_u32 v[14:15], s[58:59], v12, s65, v[14:15]
	v_mov_b32_e32 v18, v15
	v_mad_u64_u32 v[18:19], s[58:59], v13, s65, v[18:19]
	v_mov_b32_e32 v15, v18
	v_lshl_add_u64 v[14:15], v[14:15], 0, s[96:97]
	v_lshl_add_u64 v[14:15], v[14:15], 0, v[142:143]
	v_lshl_add_u64 v[14:15], v[14:15], 0, s[48:49]
	v_lshl_add_u64 v[20:21], v[14:15], 0, s[50:51]
	v_add_co_u32_e32 v14, vcc, s73, v14
	v_lshlrev_b64 v[12:13], 11, v[12:13]
	s_nop 0
	v_addc_co_u32_e32 v15, vcc, 0, v15, vcc
	global_load_dwordx2 v[64:65], v[14:15], off offset:2560
	v_lshl_add_u64 v[14:15], v[32:33], 0, v[12:13]
	ds_read_b64 v[66:67], v240 offset:4096
	s_nop 0
	global_load_dwordx2 v[68:69], v[20:21], off offset:32
	s_nop 0
	ds_read_b64 v[70:71], v240 offset:4608
	s_movk_i32 s58, 0x50
	v_or_b32_e32 v84, s58, v86
	v_lshl_add_u64 v[12:13], s[54:55], 0, v[84:85]
	v_mov_b64_e32 v[14:15], s[88:89]
	v_mad_u64_u32 v[14:15], s[58:59], v12, s65, v[14:15]
	v_mov_b32_e32 v18, v15
	v_mad_u64_u32 v[18:19], s[58:59], v13, s65, v[18:19]
	v_mov_b32_e32 v15, v18
	v_lshl_add_u64 v[14:15], v[14:15], 0, s[96:97]
	v_lshl_add_u64 v[14:15], v[14:15], 0, v[142:143]
	v_lshl_add_u64 v[14:15], v[14:15], 0, s[48:49]
	v_lshl_add_u64 v[20:21], v[14:15], 0, s[50:51]
	v_add_co_u32_e32 v14, vcc, s73, v14
	v_lshlrev_b64 v[12:13], 11, v[12:13]
	s_nop 0
	v_addc_co_u32_e32 v15, vcc, 0, v15, vcc
	global_load_dwordx2 v[72:73], v[14:15], off offset:2560
	v_lshl_add_u64 v[14:15], v[32:33], 0, v[12:13]
	ds_read_b64 v[74:75], v240 offset:5120
	s_nop 0
	global_load_dwordx2 v[76:77], v[20:21], off offset:32
	s_nop 0
	ds_read_b64 v[78:79], v240 offset:5632
	s_movk_i32 s58, 0x60
	v_or_b32_e32 v84, s58, v86
	v_lshl_add_u64 v[12:13], s[54:55], 0, v[84:85]
	v_mov_b64_e32 v[14:15], s[88:89]
	v_mad_u64_u32 v[14:15], s[58:59], v12, s65, v[14:15]
	v_mov_b32_e32 v18, v15
	v_mad_u64_u32 v[18:19], s[58:59], v13, s65, v[18:19]
	v_mov_b32_e32 v15, v18
	v_lshl_add_u64 v[14:15], v[14:15], 0, s[96:97]
	v_lshl_add_u64 v[14:15], v[14:15], 0, v[142:143]
	v_lshl_add_u64 v[14:15], v[14:15], 0, s[48:49]
	v_lshl_add_u64 v[20:21], v[14:15], 0, s[50:51]
	v_add_co_u32_e32 v14, vcc, s73, v14
	v_lshlrev_b64 v[12:13], 11, v[12:13]
	s_nop 0
	v_addc_co_u32_e32 v15, vcc, 0, v15, vcc
	global_load_dwordx2 v[200:201], v[14:15], off offset:2560
	v_lshl_add_u64 v[14:15], v[32:33], 0, v[12:13]
	ds_read_b64 v[202:203], v240 offset:6144
	s_nop 0
	global_load_dwordx2 v[204:205], v[20:21], off offset:32
	s_nop 0
	ds_read_b64 v[206:207], v240 offset:6656
	s_movk_i32 s58, 0x70
	v_or_b32_e32 v84, s58, v86
	v_lshl_add_u64 v[12:13], s[54:55], 0, v[84:85]
	v_mov_b64_e32 v[14:15], s[88:89]
	v_mad_u64_u32 v[14:15], s[58:59], v12, s65, v[14:15]
	v_mov_b32_e32 v18, v15
	v_mad_u64_u32 v[18:19], s[58:59], v13, s65, v[18:19]
	v_mov_b32_e32 v15, v18
	v_lshl_add_u64 v[14:15], v[14:15], 0, s[96:97]
	v_lshl_add_u64 v[14:15], v[14:15], 0, v[142:143]
	v_lshl_add_u64 v[14:15], v[14:15], 0, s[48:49]
	v_lshl_add_u64 v[20:21], v[14:15], 0, s[50:51]
	v_add_co_u32_e32 v14, vcc, s73, v14
	v_lshlrev_b64 v[12:13], 11, v[12:13]
	s_nop 0
	v_addc_co_u32_e32 v15, vcc, 0, v15, vcc
	global_load_dwordx2 v[208:209], v[14:15], off offset:2560
	v_lshl_add_u64 v[14:15], v[32:33], 0, v[12:13]
	ds_read_b64 v[210:211], v240 offset:7168
	s_nop 0
	global_load_dwordx2 v[212:213], v[20:21], off offset:32
	s_nop 0
	ds_read_b64 v[214:215], v240 offset:7680
	s_barrier
	s_waitcnt vmcnt(15)
	v_mov_b32_e32 v8, v1
	v_mov_b32_e32 v9, v3
	v_mov_b32_e32 v1, v2
	s_waitcnt vmcnt(14)
	v_mov_b32_e32 v2, v5
	v_mov_b32_e32 v3, v7
	v_mov_b32_e32 v5, v6
	v_lshl_add_u64 v[6:7], v[10:11], 0, s[48:49]
	v_lshl_add_u64 v[10:11], v[134:135], 0, v[144:145]
	s_waitcnt vmcnt(14)
	v_add_u32_e32 v28, -16, v29
	ds_read_b128 v[30:33], v28
	ds_read_b128 v[34:37], v29
	s_mov_b32 s58, 0x800000
	s_waitcnt lgkmcnt(1)
	v_mov_b32_e32 v38, v31
	v_mov_b32_e32 v39, v32
	v_mov_b32_e32 v31, v33
	v_pk_add_f32 v[30:31], v[38:39], v[30:31]
	s_waitcnt lgkmcnt(0)
	v_mov_b32_e32 v32, v36
	v_mov_b32_e32 v33, v34
	v_mov_b32_e32 v34, v37
	v_pk_add_f32 v[32:33], v[32:33], v[34:35]
	v_add_f32_e32 v28, v30, v31
	v_add_f32_e32 v28, v28, v33
	v_add_f32_e32 v28, v32, v28
	v_fmamk_f32 v28, v28, 0x3b800000, v195
	v_cmp_gt_f32_e32 vcc, s58, v28
	v_mul_f32_e32 v30, 0x4b800000, v28
	v_lshlrev_b32_e32 v33, 16, v27
	v_cndmask_b32_e32 v28, v28, v30, vcc
	v_rsq_f32_e32 v28, v28
	v_lshlrev_b32_e32 v32, 16, v26
	v_and_b32_e32 v27, 0xffff0000, v27
	v_and_b32_e32 v26, 0xffff0000, v26
	v_mul_f32_e32 v30, 0x45800000, v28
	v_cndmask_b32_e32 v28, v28, v30, vcc
	v_pk_mul_f32 v[32:33], v[28:29], v[32:33] op_sel_hi:[0,1]
	v_pk_mul_f32 v[32:33], v[0:1], v[32:33]
	v_lshlrev_b32_e32 v35, 16, v23
	v_lshlrev_b32_e32 v34, 16, v22
	v_pk_mul_f32 v[26:27], v[28:29], v[26:27] op_sel_hi:[0,1]
	v_pk_mul_f32 v[32:33], v[32:33], v[34:35]
	v_pk_mul_f32 v[26:27], v[8:9], v[26:27]
	v_and_b32_e32 v23, 0xffff0000, v23
	v_and_b32_e32 v22, 0xffff0000, v22
	v_pk_mul_f32 v[22:23], v[26:27], v[22:23]
	v_and_b32_sdwa v27, v32, v198 dst_sel:DWORD dst_unused:UNUSED_PAD src0_sel:WORD_1 src1_sel:DWORD
	v_and_b32_sdwa v26, v33, v198 dst_sel:DWORD dst_unused:UNUSED_PAD src0_sel:WORD_1 src1_sel:DWORD
	v_add3_u32 v27, v32, v27, s71
	v_and_b32_sdwa v32, v23, v198 dst_sel:DWORD dst_unused:UNUSED_PAD src0_sel:WORD_1 src1_sel:DWORD
	v_add3_u32 v26, v33, v26, s71
	v_and_b32_sdwa v33, v22, v198 dst_sel:DWORD dst_unused:UNUSED_PAD src0_sel:WORD_1 src1_sel:DWORD
	v_add3_u32 v23, v23, v32, s71
	v_lshl_add_u64 v[30:31], v[10:11], 0, s[56:57]
	v_add3_u32 v22, v22, v33, s71
	v_and_b32_e32 v23, 0xffff0000, v23
	v_and_b32_e32 v22, 0xffff0000, v22
	v_or_b32_sdwa v23, v23, v26 dst_sel:DWORD dst_unused:UNUSED_PAD src0_sel:DWORD src1_sel:WORD_1
	v_add_co_u32_e32 v26, vcc, s72, v30
	v_or_b32_sdwa v22, v22, v27 dst_sel:DWORD dst_unused:UNUSED_PAD src0_sel:DWORD src1_sel:WORD_1
	s_nop 0
	v_addc_co_u32_e32 v27, vcc, 0, v31, vcc
	global_store_dwordx2 v[26:27], v[22:23], off offset:3072
	v_lshlrev_b32_e32 v23, 16, v25
	v_lshlrev_b32_e32 v22, 16, v24
	v_pk_mul_f32 v[22:23], v[28:29], v[22:23] op_sel_hi:[0,1]
	v_and_b32_e32 v25, 0xffff0000, v25
	v_and_b32_e32 v24, 0xffff0000, v24
	v_pk_mul_f32 v[22:23], v[4:5], v[22:23]
	v_lshlrev_b32_e32 v31, 16, v17
	v_lshlrev_b32_e32 v30, 16, v16
	v_pk_mul_f32 v[24:25], v[28:29], v[24:25] op_sel_hi:[0,1]
	v_pk_mul_f32 v[22:23], v[22:23], v[30:31]
	v_pk_mul_f32 v[24:25], v[2:3], v[24:25]
	v_and_b32_e32 v17, 0xffff0000, v17
	v_and_b32_e32 v16, 0xffff0000, v16
	v_pk_mul_f32 v[16:17], v[24:25], v[16:17]
	v_and_b32_sdwa v24, v23, v198 dst_sel:DWORD dst_unused:UNUSED_PAD src0_sel:WORD_1 src1_sel:DWORD
	v_and_b32_sdwa v25, v22, v198 dst_sel:DWORD dst_unused:UNUSED_PAD src0_sel:WORD_1 src1_sel:DWORD
	v_add3_u32 v22, v22, v25, s71
	v_add3_u32 v23, v23, v24, s71
	v_and_b32_sdwa v24, v17, v198 dst_sel:DWORD dst_unused:UNUSED_PAD src0_sel:WORD_1 src1_sel:DWORD
	v_and_b32_sdwa v25, v16, v198 dst_sel:DWORD dst_unused:UNUSED_PAD src0_sel:WORD_1 src1_sel:DWORD
	v_add3_u32 v17, v17, v24, s71
	v_add3_u32 v16, v16, v25, s71
	v_and_b32_e32 v17, 0xffff0000, v17
	v_and_b32_e32 v16, 0xffff0000, v16
	s_add_u32 s56, s56, 0x8000
	v_or_b32_sdwa v17, v17, v23 dst_sel:DWORD dst_unused:UNUSED_PAD src0_sel:DWORD src1_sel:WORD_1
	v_or_b32_sdwa v16, v16, v22 dst_sel:DWORD dst_unused:UNUSED_PAD src0_sel:DWORD src1_sel:WORD_1
	s_addc_u32 s57, s57, 0
	global_store_dwordx2 v[26:27], v[16:17], off offset:3104
	v_add_u32_e32 v29, 0x200, v29
	s_waitcnt vmcnt(14)
	v_add_u32_e32 v28, -16, v29
	ds_read_b128 v[30:33], v28
	ds_read_b128 v[34:37], v29
	s_mov_b32 s58, 0x800000
	s_waitcnt lgkmcnt(1)
	v_mov_b32_e32 v38, v31
	v_mov_b32_e32 v39, v32
	v_mov_b32_e32 v31, v33
	v_pk_add_f32 v[30:31], v[38:39], v[30:31]
	s_waitcnt lgkmcnt(0)
	v_mov_b32_e32 v32, v36
	v_mov_b32_e32 v33, v34
	v_mov_b32_e32 v34, v37
	v_pk_add_f32 v[32:33], v[32:33], v[34:35]
	v_add_f32_e32 v28, v30, v31
	v_add_f32_e32 v28, v28, v33
	v_add_f32_e32 v28, v32, v28
	v_fmamk_f32 v28, v28, 0x3b800000, v195
	v_cmp_gt_f32_e32 vcc, s58, v28
	v_mul_f32_e32 v30, 0x4b800000, v28
	v_lshlrev_b32_e32 v33, 16, v43
	v_cndmask_b32_e32 v28, v28, v30, vcc
	v_rsq_f32_e32 v28, v28
	v_lshlrev_b32_e32 v32, 16, v42
	v_and_b32_e32 v43, 0xffff0000, v43
	v_and_b32_e32 v42, 0xffff0000, v42
	v_mul_f32_e32 v30, 0x45800000, v28
	v_cndmask_b32_e32 v28, v28, v30, vcc
	v_pk_mul_f32 v[32:33], v[28:29], v[32:33] op_sel_hi:[0,1]
	v_pk_mul_f32 v[32:33], v[0:1], v[32:33]
	v_lshlrev_b32_e32 v35, 16, v41
	v_lshlrev_b32_e32 v34, 16, v40
	v_pk_mul_f32 v[42:43], v[28:29], v[42:43] op_sel_hi:[0,1]
	v_pk_mul_f32 v[32:33], v[32:33], v[34:35]
	v_pk_mul_f32 v[42:43], v[8:9], v[42:43]
	v_and_b32_e32 v41, 0xffff0000, v41
	v_and_b32_e32 v40, 0xffff0000, v40
	v_pk_mul_f32 v[40:41], v[42:43], v[40:41]
	v_and_b32_sdwa v43, v32, v198 dst_sel:DWORD dst_unused:UNUSED_PAD src0_sel:WORD_1 src1_sel:DWORD
	v_and_b32_sdwa v42, v33, v198 dst_sel:DWORD dst_unused:UNUSED_PAD src0_sel:WORD_1 src1_sel:DWORD
	v_add3_u32 v43, v32, v43, s71
	v_and_b32_sdwa v32, v41, v198 dst_sel:DWORD dst_unused:UNUSED_PAD src0_sel:WORD_1 src1_sel:DWORD
	v_add3_u32 v42, v33, v42, s71
	v_and_b32_sdwa v33, v40, v198 dst_sel:DWORD dst_unused:UNUSED_PAD src0_sel:WORD_1 src1_sel:DWORD
	v_add3_u32 v41, v41, v32, s71
	v_lshl_add_u64 v[30:31], v[10:11], 0, s[56:57]
	v_add3_u32 v40, v40, v33, s71
	v_and_b32_e32 v41, 0xffff0000, v41
	v_and_b32_e32 v40, 0xffff0000, v40
	v_or_b32_sdwa v41, v41, v42 dst_sel:DWORD dst_unused:UNUSED_PAD src0_sel:DWORD src1_sel:WORD_1
	v_add_co_u32_e32 v42, vcc, s72, v30
	v_or_b32_sdwa v40, v40, v43 dst_sel:DWORD dst_unused:UNUSED_PAD src0_sel:DWORD src1_sel:WORD_1
	s_nop 0
	v_addc_co_u32_e32 v43, vcc, 0, v31, vcc
	global_store_dwordx2 v[42:43], v[40:41], off offset:3072
	v_lshlrev_b32_e32 v41, 16, v47
	v_lshlrev_b32_e32 v40, 16, v46
	v_pk_mul_f32 v[40:41], v[28:29], v[40:41] op_sel_hi:[0,1]
	v_and_b32_e32 v47, 0xffff0000, v47
	v_and_b32_e32 v46, 0xffff0000, v46
	v_pk_mul_f32 v[40:41], v[4:5], v[40:41]
	v_lshlrev_b32_e32 v31, 16, v45
	v_lshlrev_b32_e32 v30, 16, v44
	v_pk_mul_f32 v[46:47], v[28:29], v[46:47] op_sel_hi:[0,1]
	v_pk_mul_f32 v[40:41], v[40:41], v[30:31]
	v_pk_mul_f32 v[46:47], v[2:3], v[46:47]
	v_and_b32_e32 v45, 0xffff0000, v45
	v_and_b32_e32 v44, 0xffff0000, v44
	v_pk_mul_f32 v[44:45], v[46:47], v[44:45]
	v_and_b32_sdwa v46, v41, v198 dst_sel:DWORD dst_unused:UNUSED_PAD src0_sel:WORD_1 src1_sel:DWORD
	v_and_b32_sdwa v47, v40, v198 dst_sel:DWORD dst_unused:UNUSED_PAD src0_sel:WORD_1 src1_sel:DWORD
	v_add3_u32 v40, v40, v47, s71
	v_add3_u32 v41, v41, v46, s71
	v_and_b32_sdwa v46, v45, v198 dst_sel:DWORD dst_unused:UNUSED_PAD src0_sel:WORD_1 src1_sel:DWORD
	v_and_b32_sdwa v47, v44, v198 dst_sel:DWORD dst_unused:UNUSED_PAD src0_sel:WORD_1 src1_sel:DWORD
	v_add3_u32 v45, v45, v46, s71
	v_add3_u32 v44, v44, v47, s71
	v_and_b32_e32 v45, 0xffff0000, v45
	v_and_b32_e32 v44, 0xffff0000, v44
	s_add_u32 s56, s56, 0x8000
	v_or_b32_sdwa v45, v45, v41 dst_sel:DWORD dst_unused:UNUSED_PAD src0_sel:DWORD src1_sel:WORD_1
	v_or_b32_sdwa v44, v44, v40 dst_sel:DWORD dst_unused:UNUSED_PAD src0_sel:DWORD src1_sel:WORD_1
	s_addc_u32 s57, s57, 0
	global_store_dwordx2 v[42:43], v[44:45], off offset:3104
	v_add_u32_e32 v29, 0x200, v29
	s_waitcnt vmcnt(14)
	v_add_u32_e32 v28, -16, v29
	ds_read_b128 v[30:33], v28
	ds_read_b128 v[34:37], v29
	s_mov_b32 s58, 0x800000
	s_waitcnt lgkmcnt(1)
	v_mov_b32_e32 v38, v31
	v_mov_b32_e32 v39, v32
	v_mov_b32_e32 v31, v33
	v_pk_add_f32 v[30:31], v[38:39], v[30:31]
	s_waitcnt lgkmcnt(0)
	v_mov_b32_e32 v32, v36
	v_mov_b32_e32 v33, v34
	v_mov_b32_e32 v34, v37
	v_pk_add_f32 v[32:33], v[32:33], v[34:35]
	v_add_f32_e32 v28, v30, v31
	v_add_f32_e32 v28, v28, v33
	v_add_f32_e32 v28, v32, v28
	v_fmamk_f32 v28, v28, 0x3b800000, v195
	v_cmp_gt_f32_e32 vcc, s58, v28
	v_mul_f32_e32 v30, 0x4b800000, v28
	v_lshlrev_b32_e32 v33, 16, v51
	v_cndmask_b32_e32 v28, v28, v30, vcc
	v_rsq_f32_e32 v28, v28
	v_lshlrev_b32_e32 v32, 16, v50
	v_and_b32_e32 v51, 0xffff0000, v51
	v_and_b32_e32 v50, 0xffff0000, v50
	v_mul_f32_e32 v30, 0x45800000, v28
	v_cndmask_b32_e32 v28, v28, v30, vcc
	v_pk_mul_f32 v[32:33], v[28:29], v[32:33] op_sel_hi:[0,1]
	v_pk_mul_f32 v[32:33], v[0:1], v[32:33]
	v_lshlrev_b32_e32 v35, 16, v49
	v_lshlrev_b32_e32 v34, 16, v48
	v_pk_mul_f32 v[50:51], v[28:29], v[50:51] op_sel_hi:[0,1]
	v_pk_mul_f32 v[32:33], v[32:33], v[34:35]
	v_pk_mul_f32 v[50:51], v[8:9], v[50:51]
	v_and_b32_e32 v49, 0xffff0000, v49
	v_and_b32_e32 v48, 0xffff0000, v48
	v_pk_mul_f32 v[48:49], v[50:51], v[48:49]
	v_and_b32_sdwa v51, v32, v198 dst_sel:DWORD dst_unused:UNUSED_PAD src0_sel:WORD_1 src1_sel:DWORD
	v_and_b32_sdwa v50, v33, v198 dst_sel:DWORD dst_unused:UNUSED_PAD src0_sel:WORD_1 src1_sel:DWORD
	v_add3_u32 v51, v32, v51, s71
	v_and_b32_sdwa v32, v49, v198 dst_sel:DWORD dst_unused:UNUSED_PAD src0_sel:WORD_1 src1_sel:DWORD
	v_add3_u32 v50, v33, v50, s71
	v_and_b32_sdwa v33, v48, v198 dst_sel:DWORD dst_unused:UNUSED_PAD src0_sel:WORD_1 src1_sel:DWORD
	v_add3_u32 v49, v49, v32, s71
	v_lshl_add_u64 v[30:31], v[10:11], 0, s[56:57]
	v_add3_u32 v48, v48, v33, s71
	v_and_b32_e32 v49, 0xffff0000, v49
	v_and_b32_e32 v48, 0xffff0000, v48
	v_or_b32_sdwa v49, v49, v50 dst_sel:DWORD dst_unused:UNUSED_PAD src0_sel:DWORD src1_sel:WORD_1
	v_add_co_u32_e32 v50, vcc, s72, v30
	v_or_b32_sdwa v48, v48, v51 dst_sel:DWORD dst_unused:UNUSED_PAD src0_sel:DWORD src1_sel:WORD_1
	s_nop 0
	v_addc_co_u32_e32 v51, vcc, 0, v31, vcc
	global_store_dwordx2 v[50:51], v[48:49], off offset:3072
	v_lshlrev_b32_e32 v49, 16, v55
	v_lshlrev_b32_e32 v48, 16, v54
	v_pk_mul_f32 v[48:49], v[28:29], v[48:49] op_sel_hi:[0,1]
	v_and_b32_e32 v55, 0xffff0000, v55
	v_and_b32_e32 v54, 0xffff0000, v54
	v_pk_mul_f32 v[48:49], v[4:5], v[48:49]
	v_lshlrev_b32_e32 v31, 16, v53
	v_lshlrev_b32_e32 v30, 16, v52
	v_pk_mul_f32 v[54:55], v[28:29], v[54:55] op_sel_hi:[0,1]
	v_pk_mul_f32 v[48:49], v[48:49], v[30:31]
	v_pk_mul_f32 v[54:55], v[2:3], v[54:55]
	v_and_b32_e32 v53, 0xffff0000, v53
	v_and_b32_e32 v52, 0xffff0000, v52
	v_pk_mul_f32 v[52:53], v[54:55], v[52:53]
	v_and_b32_sdwa v54, v49, v198 dst_sel:DWORD dst_unused:UNUSED_PAD src0_sel:WORD_1 src1_sel:DWORD
	v_and_b32_sdwa v55, v48, v198 dst_sel:DWORD dst_unused:UNUSED_PAD src0_sel:WORD_1 src1_sel:DWORD
	v_add3_u32 v48, v48, v55, s71
	v_add3_u32 v49, v49, v54, s71
	v_and_b32_sdwa v54, v53, v198 dst_sel:DWORD dst_unused:UNUSED_PAD src0_sel:WORD_1 src1_sel:DWORD
	v_and_b32_sdwa v55, v52, v198 dst_sel:DWORD dst_unused:UNUSED_PAD src0_sel:WORD_1 src1_sel:DWORD
	v_add3_u32 v53, v53, v54, s71
	v_add3_u32 v52, v52, v55, s71
	v_and_b32_e32 v53, 0xffff0000, v53
	v_and_b32_e32 v52, 0xffff0000, v52
	s_add_u32 s56, s56, 0x8000
	v_or_b32_sdwa v53, v53, v49 dst_sel:DWORD dst_unused:UNUSED_PAD src0_sel:DWORD src1_sel:WORD_1
	v_or_b32_sdwa v52, v52, v48 dst_sel:DWORD dst_unused:UNUSED_PAD src0_sel:DWORD src1_sel:WORD_1
	s_addc_u32 s57, s57, 0
	global_store_dwordx2 v[50:51], v[52:53], off offset:3104
	v_add_u32_e32 v29, 0x200, v29
	s_waitcnt vmcnt(14)
	v_add_u32_e32 v28, -16, v29
	ds_read_b128 v[30:33], v28
	ds_read_b128 v[34:37], v29
	s_mov_b32 s58, 0x800000
	s_waitcnt lgkmcnt(1)
	v_mov_b32_e32 v38, v31
	v_mov_b32_e32 v39, v32
	v_mov_b32_e32 v31, v33
	v_pk_add_f32 v[30:31], v[38:39], v[30:31]
	s_waitcnt lgkmcnt(0)
	v_mov_b32_e32 v32, v36
	v_mov_b32_e32 v33, v34
	v_mov_b32_e32 v34, v37
	v_pk_add_f32 v[32:33], v[32:33], v[34:35]
	v_add_f32_e32 v28, v30, v31
	v_add_f32_e32 v28, v28, v33
	v_add_f32_e32 v28, v32, v28
	v_fmamk_f32 v28, v28, 0x3b800000, v195
	v_cmp_gt_f32_e32 vcc, s58, v28
	v_mul_f32_e32 v30, 0x4b800000, v28
	v_lshlrev_b32_e32 v33, 16, v59
	v_cndmask_b32_e32 v28, v28, v30, vcc
	v_rsq_f32_e32 v28, v28
	v_lshlrev_b32_e32 v32, 16, v58
	v_and_b32_e32 v59, 0xffff0000, v59
	v_and_b32_e32 v58, 0xffff0000, v58
	v_mul_f32_e32 v30, 0x45800000, v28
	v_cndmask_b32_e32 v28, v28, v30, vcc
	v_pk_mul_f32 v[32:33], v[28:29], v[32:33] op_sel_hi:[0,1]
	v_pk_mul_f32 v[32:33], v[0:1], v[32:33]
	v_lshlrev_b32_e32 v35, 16, v57
	v_lshlrev_b32_e32 v34, 16, v56
	v_pk_mul_f32 v[58:59], v[28:29], v[58:59] op_sel_hi:[0,1]
	v_pk_mul_f32 v[32:33], v[32:33], v[34:35]
	v_pk_mul_f32 v[58:59], v[8:9], v[58:59]
	v_and_b32_e32 v57, 0xffff0000, v57
	v_and_b32_e32 v56, 0xffff0000, v56
	v_pk_mul_f32 v[56:57], v[58:59], v[56:57]
	v_and_b32_sdwa v59, v32, v198 dst_sel:DWORD dst_unused:UNUSED_PAD src0_sel:WORD_1 src1_sel:DWORD
	v_and_b32_sdwa v58, v33, v198 dst_sel:DWORD dst_unused:UNUSED_PAD src0_sel:WORD_1 src1_sel:DWORD
	v_add3_u32 v59, v32, v59, s71
	v_and_b32_sdwa v32, v57, v198 dst_sel:DWORD dst_unused:UNUSED_PAD src0_sel:WORD_1 src1_sel:DWORD
	v_add3_u32 v58, v33, v58, s71
	v_and_b32_sdwa v33, v56, v198 dst_sel:DWORD dst_unused:UNUSED_PAD src0_sel:WORD_1 src1_sel:DWORD
	v_add3_u32 v57, v57, v32, s71
	v_lshl_add_u64 v[30:31], v[10:11], 0, s[56:57]
	v_add3_u32 v56, v56, v33, s71
	v_and_b32_e32 v57, 0xffff0000, v57
	v_and_b32_e32 v56, 0xffff0000, v56
	v_or_b32_sdwa v57, v57, v58 dst_sel:DWORD dst_unused:UNUSED_PAD src0_sel:DWORD src1_sel:WORD_1
	v_add_co_u32_e32 v58, vcc, s72, v30
	v_or_b32_sdwa v56, v56, v59 dst_sel:DWORD dst_unused:UNUSED_PAD src0_sel:DWORD src1_sel:WORD_1
	s_nop 0
	v_addc_co_u32_e32 v59, vcc, 0, v31, vcc
	global_store_dwordx2 v[58:59], v[56:57], off offset:3072
	v_lshlrev_b32_e32 v57, 16, v63
	v_lshlrev_b32_e32 v56, 16, v62
	v_pk_mul_f32 v[56:57], v[28:29], v[56:57] op_sel_hi:[0,1]
	v_and_b32_e32 v63, 0xffff0000, v63
	v_and_b32_e32 v62, 0xffff0000, v62
	v_pk_mul_f32 v[56:57], v[4:5], v[56:57]
	v_lshlrev_b32_e32 v31, 16, v61
	v_lshlrev_b32_e32 v30, 16, v60
	v_pk_mul_f32 v[62:63], v[28:29], v[62:63] op_sel_hi:[0,1]
	v_pk_mul_f32 v[56:57], v[56:57], v[30:31]
	v_pk_mul_f32 v[62:63], v[2:3], v[62:63]
	v_and_b32_e32 v61, 0xffff0000, v61
	v_and_b32_e32 v60, 0xffff0000, v60
	v_pk_mul_f32 v[60:61], v[62:63], v[60:61]
	v_and_b32_sdwa v62, v57, v198 dst_sel:DWORD dst_unused:UNUSED_PAD src0_sel:WORD_1 src1_sel:DWORD
	v_and_b32_sdwa v63, v56, v198 dst_sel:DWORD dst_unused:UNUSED_PAD src0_sel:WORD_1 src1_sel:DWORD
	v_add3_u32 v56, v56, v63, s71
	v_add3_u32 v57, v57, v62, s71
	v_and_b32_sdwa v62, v61, v198 dst_sel:DWORD dst_unused:UNUSED_PAD src0_sel:WORD_1 src1_sel:DWORD
	v_and_b32_sdwa v63, v60, v198 dst_sel:DWORD dst_unused:UNUSED_PAD src0_sel:WORD_1 src1_sel:DWORD
	v_add3_u32 v61, v61, v62, s71
	v_add3_u32 v60, v60, v63, s71
	v_and_b32_e32 v61, 0xffff0000, v61
	v_and_b32_e32 v60, 0xffff0000, v60
	s_add_u32 s56, s56, 0x8000
	v_or_b32_sdwa v61, v61, v57 dst_sel:DWORD dst_unused:UNUSED_PAD src0_sel:DWORD src1_sel:WORD_1
	v_or_b32_sdwa v60, v60, v56 dst_sel:DWORD dst_unused:UNUSED_PAD src0_sel:DWORD src1_sel:WORD_1
	s_addc_u32 s57, s57, 0
	global_store_dwordx2 v[58:59], v[60:61], off offset:3104
	v_add_u32_e32 v29, 0x200, v29
	s_waitcnt vmcnt(14)
	v_add_u32_e32 v28, -16, v29
	ds_read_b128 v[30:33], v28
	ds_read_b128 v[34:37], v29
	s_mov_b32 s58, 0x800000
	s_waitcnt lgkmcnt(1)
	v_mov_b32_e32 v38, v31
	v_mov_b32_e32 v39, v32
	v_mov_b32_e32 v31, v33
	v_pk_add_f32 v[30:31], v[38:39], v[30:31]
	s_waitcnt lgkmcnt(0)
	v_mov_b32_e32 v32, v36
	v_mov_b32_e32 v33, v34
	v_mov_b32_e32 v34, v37
	v_pk_add_f32 v[32:33], v[32:33], v[34:35]
	v_add_f32_e32 v28, v30, v31
	v_add_f32_e32 v28, v28, v33
	v_add_f32_e32 v28, v32, v28
	v_fmamk_f32 v28, v28, 0x3b800000, v195
	v_cmp_gt_f32_e32 vcc, s58, v28
	v_mul_f32_e32 v30, 0x4b800000, v28
	v_lshlrev_b32_e32 v33, 16, v67
	v_cndmask_b32_e32 v28, v28, v30, vcc
	v_rsq_f32_e32 v28, v28
	v_lshlrev_b32_e32 v32, 16, v66
	v_and_b32_e32 v67, 0xffff0000, v67
	v_and_b32_e32 v66, 0xffff0000, v66
	v_mul_f32_e32 v30, 0x45800000, v28
	v_cndmask_b32_e32 v28, v28, v30, vcc
	v_pk_mul_f32 v[32:33], v[28:29], v[32:33] op_sel_hi:[0,1]
	v_pk_mul_f32 v[32:33], v[0:1], v[32:33]
	v_lshlrev_b32_e32 v35, 16, v65
	v_lshlrev_b32_e32 v34, 16, v64
	v_pk_mul_f32 v[66:67], v[28:29], v[66:67] op_sel_hi:[0,1]
	v_pk_mul_f32 v[32:33], v[32:33], v[34:35]
	v_pk_mul_f32 v[66:67], v[8:9], v[66:67]
	v_and_b32_e32 v65, 0xffff0000, v65
	v_and_b32_e32 v64, 0xffff0000, v64
	v_pk_mul_f32 v[64:65], v[66:67], v[64:65]
	v_and_b32_sdwa v67, v32, v198 dst_sel:DWORD dst_unused:UNUSED_PAD src0_sel:WORD_1 src1_sel:DWORD
	v_and_b32_sdwa v66, v33, v198 dst_sel:DWORD dst_unused:UNUSED_PAD src0_sel:WORD_1 src1_sel:DWORD
	v_add3_u32 v67, v32, v67, s71
	v_and_b32_sdwa v32, v65, v198 dst_sel:DWORD dst_unused:UNUSED_PAD src0_sel:WORD_1 src1_sel:DWORD
	v_add3_u32 v66, v33, v66, s71
	v_and_b32_sdwa v33, v64, v198 dst_sel:DWORD dst_unused:UNUSED_PAD src0_sel:WORD_1 src1_sel:DWORD
	v_add3_u32 v65, v65, v32, s71
	v_lshl_add_u64 v[30:31], v[10:11], 0, s[56:57]
	v_add3_u32 v64, v64, v33, s71
	v_and_b32_e32 v65, 0xffff0000, v65
	v_and_b32_e32 v64, 0xffff0000, v64
	v_or_b32_sdwa v65, v65, v66 dst_sel:DWORD dst_unused:UNUSED_PAD src0_sel:DWORD src1_sel:WORD_1
	v_add_co_u32_e32 v66, vcc, s72, v30
	v_or_b32_sdwa v64, v64, v67 dst_sel:DWORD dst_unused:UNUSED_PAD src0_sel:DWORD src1_sel:WORD_1
	s_nop 0
	v_addc_co_u32_e32 v67, vcc, 0, v31, vcc
	global_store_dwordx2 v[66:67], v[64:65], off offset:3072
	v_lshlrev_b32_e32 v65, 16, v71
	v_lshlrev_b32_e32 v64, 16, v70
	v_pk_mul_f32 v[64:65], v[28:29], v[64:65] op_sel_hi:[0,1]
	v_and_b32_e32 v71, 0xffff0000, v71
	v_and_b32_e32 v70, 0xffff0000, v70
	v_pk_mul_f32 v[64:65], v[4:5], v[64:65]
	v_lshlrev_b32_e32 v31, 16, v69
	v_lshlrev_b32_e32 v30, 16, v68
	v_pk_mul_f32 v[70:71], v[28:29], v[70:71] op_sel_hi:[0,1]
	v_pk_mul_f32 v[64:65], v[64:65], v[30:31]
	v_pk_mul_f32 v[70:71], v[2:3], v[70:71]
	v_and_b32_e32 v69, 0xffff0000, v69
	v_and_b32_e32 v68, 0xffff0000, v68
	v_pk_mul_f32 v[68:69], v[70:71], v[68:69]
	v_and_b32_sdwa v70, v65, v198 dst_sel:DWORD dst_unused:UNUSED_PAD src0_sel:WORD_1 src1_sel:DWORD
	v_and_b32_sdwa v71, v64, v198 dst_sel:DWORD dst_unused:UNUSED_PAD src0_sel:WORD_1 src1_sel:DWORD
	v_add3_u32 v64, v64, v71, s71
	v_add3_u32 v65, v65, v70, s71
	v_and_b32_sdwa v70, v69, v198 dst_sel:DWORD dst_unused:UNUSED_PAD src0_sel:WORD_1 src1_sel:DWORD
	v_and_b32_sdwa v71, v68, v198 dst_sel:DWORD dst_unused:UNUSED_PAD src0_sel:WORD_1 src1_sel:DWORD
	v_add3_u32 v69, v69, v70, s71
	v_add3_u32 v68, v68, v71, s71
	v_and_b32_e32 v69, 0xffff0000, v69
	v_and_b32_e32 v68, 0xffff0000, v68
	s_add_u32 s56, s56, 0x8000
	v_or_b32_sdwa v69, v69, v65 dst_sel:DWORD dst_unused:UNUSED_PAD src0_sel:DWORD src1_sel:WORD_1
	v_or_b32_sdwa v68, v68, v64 dst_sel:DWORD dst_unused:UNUSED_PAD src0_sel:DWORD src1_sel:WORD_1
	s_addc_u32 s57, s57, 0
	global_store_dwordx2 v[66:67], v[68:69], off offset:3104
	v_add_u32_e32 v29, 0x200, v29
	s_waitcnt vmcnt(14)
	v_add_u32_e32 v28, -16, v29
	ds_read_b128 v[30:33], v28
	ds_read_b128 v[34:37], v29
	s_mov_b32 s58, 0x800000
	s_waitcnt lgkmcnt(1)
	v_mov_b32_e32 v38, v31
	v_mov_b32_e32 v39, v32
	v_mov_b32_e32 v31, v33
	v_pk_add_f32 v[30:31], v[38:39], v[30:31]
	s_waitcnt lgkmcnt(0)
	v_mov_b32_e32 v32, v36
	v_mov_b32_e32 v33, v34
	v_mov_b32_e32 v34, v37
	v_pk_add_f32 v[32:33], v[32:33], v[34:35]
	v_add_f32_e32 v28, v30, v31
	v_add_f32_e32 v28, v28, v33
	v_add_f32_e32 v28, v32, v28
	v_fmamk_f32 v28, v28, 0x3b800000, v195
	v_cmp_gt_f32_e32 vcc, s58, v28
	v_mul_f32_e32 v30, 0x4b800000, v28
	v_lshlrev_b32_e32 v33, 16, v75
	v_cndmask_b32_e32 v28, v28, v30, vcc
	v_rsq_f32_e32 v28, v28
	v_lshlrev_b32_e32 v32, 16, v74
	v_and_b32_e32 v75, 0xffff0000, v75
	v_and_b32_e32 v74, 0xffff0000, v74
	v_mul_f32_e32 v30, 0x45800000, v28
	v_cndmask_b32_e32 v28, v28, v30, vcc
	v_pk_mul_f32 v[32:33], v[28:29], v[32:33] op_sel_hi:[0,1]
	v_pk_mul_f32 v[32:33], v[0:1], v[32:33]
	v_lshlrev_b32_e32 v35, 16, v73
	v_lshlrev_b32_e32 v34, 16, v72
	v_pk_mul_f32 v[74:75], v[28:29], v[74:75] op_sel_hi:[0,1]
	v_pk_mul_f32 v[32:33], v[32:33], v[34:35]
	v_pk_mul_f32 v[74:75], v[8:9], v[74:75]
	v_and_b32_e32 v73, 0xffff0000, v73
	v_and_b32_e32 v72, 0xffff0000, v72
	v_pk_mul_f32 v[72:73], v[74:75], v[72:73]
	v_and_b32_sdwa v75, v32, v198 dst_sel:DWORD dst_unused:UNUSED_PAD src0_sel:WORD_1 src1_sel:DWORD
	v_and_b32_sdwa v74, v33, v198 dst_sel:DWORD dst_unused:UNUSED_PAD src0_sel:WORD_1 src1_sel:DWORD
	v_add3_u32 v75, v32, v75, s71
	v_and_b32_sdwa v32, v73, v198 dst_sel:DWORD dst_unused:UNUSED_PAD src0_sel:WORD_1 src1_sel:DWORD
	v_add3_u32 v74, v33, v74, s71
	v_and_b32_sdwa v33, v72, v198 dst_sel:DWORD dst_unused:UNUSED_PAD src0_sel:WORD_1 src1_sel:DWORD
	v_add3_u32 v73, v73, v32, s71
	v_lshl_add_u64 v[30:31], v[10:11], 0, s[56:57]
	v_add3_u32 v72, v72, v33, s71
	v_and_b32_e32 v73, 0xffff0000, v73
	v_and_b32_e32 v72, 0xffff0000, v72
	v_or_b32_sdwa v73, v73, v74 dst_sel:DWORD dst_unused:UNUSED_PAD src0_sel:DWORD src1_sel:WORD_1
	v_add_co_u32_e32 v74, vcc, s72, v30
	v_or_b32_sdwa v72, v72, v75 dst_sel:DWORD dst_unused:UNUSED_PAD src0_sel:DWORD src1_sel:WORD_1
	s_nop 0
	v_addc_co_u32_e32 v75, vcc, 0, v31, vcc
	global_store_dwordx2 v[74:75], v[72:73], off offset:3072
	v_lshlrev_b32_e32 v73, 16, v79
	v_lshlrev_b32_e32 v72, 16, v78
	v_pk_mul_f32 v[72:73], v[28:29], v[72:73] op_sel_hi:[0,1]
	v_and_b32_e32 v79, 0xffff0000, v79
	v_and_b32_e32 v78, 0xffff0000, v78
	v_pk_mul_f32 v[72:73], v[4:5], v[72:73]
	v_lshlrev_b32_e32 v31, 16, v77
	v_lshlrev_b32_e32 v30, 16, v76
	v_pk_mul_f32 v[78:79], v[28:29], v[78:79] op_sel_hi:[0,1]
	v_pk_mul_f32 v[72:73], v[72:73], v[30:31]
	v_pk_mul_f32 v[78:79], v[2:3], v[78:79]
	v_and_b32_e32 v77, 0xffff0000, v77
	v_and_b32_e32 v76, 0xffff0000, v76
	v_pk_mul_f32 v[76:77], v[78:79], v[76:77]
	v_and_b32_sdwa v78, v73, v198 dst_sel:DWORD dst_unused:UNUSED_PAD src0_sel:WORD_1 src1_sel:DWORD
	v_and_b32_sdwa v79, v72, v198 dst_sel:DWORD dst_unused:UNUSED_PAD src0_sel:WORD_1 src1_sel:DWORD
	v_add3_u32 v72, v72, v79, s71
	v_add3_u32 v73, v73, v78, s71
	v_and_b32_sdwa v78, v77, v198 dst_sel:DWORD dst_unused:UNUSED_PAD src0_sel:WORD_1 src1_sel:DWORD
	v_and_b32_sdwa v79, v76, v198 dst_sel:DWORD dst_unused:UNUSED_PAD src0_sel:WORD_1 src1_sel:DWORD
	v_add3_u32 v77, v77, v78, s71
	v_add3_u32 v76, v76, v79, s71
	v_and_b32_e32 v77, 0xffff0000, v77
	v_and_b32_e32 v76, 0xffff0000, v76
	s_add_u32 s56, s56, 0x8000
	v_or_b32_sdwa v77, v77, v73 dst_sel:DWORD dst_unused:UNUSED_PAD src0_sel:DWORD src1_sel:WORD_1
	v_or_b32_sdwa v76, v76, v72 dst_sel:DWORD dst_unused:UNUSED_PAD src0_sel:DWORD src1_sel:WORD_1
	s_addc_u32 s57, s57, 0
	global_store_dwordx2 v[74:75], v[76:77], off offset:3104
	v_add_u32_e32 v29, 0x200, v29
	s_waitcnt vmcnt(14)
	v_add_u32_e32 v28, -16, v29
	ds_read_b128 v[30:33], v28
	ds_read_b128 v[34:37], v29
	s_mov_b32 s58, 0x800000
	s_waitcnt lgkmcnt(1)
	v_mov_b32_e32 v38, v31
	v_mov_b32_e32 v39, v32
	v_mov_b32_e32 v31, v33
	v_pk_add_f32 v[30:31], v[38:39], v[30:31]
	s_waitcnt lgkmcnt(0)
	v_mov_b32_e32 v32, v36
	v_mov_b32_e32 v33, v34
	v_mov_b32_e32 v34, v37
	v_pk_add_f32 v[32:33], v[32:33], v[34:35]
	v_add_f32_e32 v28, v30, v31
	v_add_f32_e32 v28, v28, v33
	v_add_f32_e32 v28, v32, v28
	v_fmamk_f32 v28, v28, 0x3b800000, v195
	v_cmp_gt_f32_e32 vcc, s58, v28
	v_mul_f32_e32 v30, 0x4b800000, v28
	v_lshlrev_b32_e32 v33, 16, v203
	v_cndmask_b32_e32 v28, v28, v30, vcc
	v_rsq_f32_e32 v28, v28
	v_lshlrev_b32_e32 v32, 16, v202
	v_and_b32_e32 v203, 0xffff0000, v203
	v_and_b32_e32 v202, 0xffff0000, v202
	v_mul_f32_e32 v30, 0x45800000, v28
	v_cndmask_b32_e32 v28, v28, v30, vcc
	v_pk_mul_f32 v[32:33], v[28:29], v[32:33] op_sel_hi:[0,1]
	v_pk_mul_f32 v[32:33], v[0:1], v[32:33]
	v_lshlrev_b32_e32 v35, 16, v201
	v_lshlrev_b32_e32 v34, 16, v200
	v_pk_mul_f32 v[202:203], v[28:29], v[202:203] op_sel_hi:[0,1]
	v_pk_mul_f32 v[32:33], v[32:33], v[34:35]
	v_pk_mul_f32 v[202:203], v[8:9], v[202:203]
	v_and_b32_e32 v201, 0xffff0000, v201
	v_and_b32_e32 v200, 0xffff0000, v200
	v_pk_mul_f32 v[200:201], v[202:203], v[200:201]
	v_and_b32_sdwa v203, v32, v198 dst_sel:DWORD dst_unused:UNUSED_PAD src0_sel:WORD_1 src1_sel:DWORD
	v_and_b32_sdwa v202, v33, v198 dst_sel:DWORD dst_unused:UNUSED_PAD src0_sel:WORD_1 src1_sel:DWORD
	v_add3_u32 v203, v32, v203, s71
	v_and_b32_sdwa v32, v201, v198 dst_sel:DWORD dst_unused:UNUSED_PAD src0_sel:WORD_1 src1_sel:DWORD
	v_add3_u32 v202, v33, v202, s71
	v_and_b32_sdwa v33, v200, v198 dst_sel:DWORD dst_unused:UNUSED_PAD src0_sel:WORD_1 src1_sel:DWORD
	v_add3_u32 v201, v201, v32, s71
	v_lshl_add_u64 v[30:31], v[10:11], 0, s[56:57]
	v_add3_u32 v200, v200, v33, s71
	v_and_b32_e32 v201, 0xffff0000, v201
	v_and_b32_e32 v200, 0xffff0000, v200
	v_or_b32_sdwa v201, v201, v202 dst_sel:DWORD dst_unused:UNUSED_PAD src0_sel:DWORD src1_sel:WORD_1
	v_add_co_u32_e32 v202, vcc, s72, v30
	v_or_b32_sdwa v200, v200, v203 dst_sel:DWORD dst_unused:UNUSED_PAD src0_sel:DWORD src1_sel:WORD_1
	s_nop 0
	v_addc_co_u32_e32 v203, vcc, 0, v31, vcc
	global_store_dwordx2 v[202:203], v[200:201], off offset:3072
	v_lshlrev_b32_e32 v201, 16, v207
	v_lshlrev_b32_e32 v200, 16, v206
	v_pk_mul_f32 v[200:201], v[28:29], v[200:201] op_sel_hi:[0,1]
	v_and_b32_e32 v207, 0xffff0000, v207
	v_and_b32_e32 v206, 0xffff0000, v206
	v_pk_mul_f32 v[200:201], v[4:5], v[200:201]
	v_lshlrev_b32_e32 v31, 16, v205
	v_lshlrev_b32_e32 v30, 16, v204
	v_pk_mul_f32 v[206:207], v[28:29], v[206:207] op_sel_hi:[0,1]
	v_pk_mul_f32 v[200:201], v[200:201], v[30:31]
	v_pk_mul_f32 v[206:207], v[2:3], v[206:207]
	v_and_b32_e32 v205, 0xffff0000, v205
	v_and_b32_e32 v204, 0xffff0000, v204
	v_pk_mul_f32 v[204:205], v[206:207], v[204:205]
	v_and_b32_sdwa v206, v201, v198 dst_sel:DWORD dst_unused:UNUSED_PAD src0_sel:WORD_1 src1_sel:DWORD
	v_and_b32_sdwa v207, v200, v198 dst_sel:DWORD dst_unused:UNUSED_PAD src0_sel:WORD_1 src1_sel:DWORD
	v_add3_u32 v200, v200, v207, s71
	v_add3_u32 v201, v201, v206, s71
	v_and_b32_sdwa v206, v205, v198 dst_sel:DWORD dst_unused:UNUSED_PAD src0_sel:WORD_1 src1_sel:DWORD
	v_and_b32_sdwa v207, v204, v198 dst_sel:DWORD dst_unused:UNUSED_PAD src0_sel:WORD_1 src1_sel:DWORD
	v_add3_u32 v205, v205, v206, s71
	v_add3_u32 v204, v204, v207, s71
	v_and_b32_e32 v205, 0xffff0000, v205
	v_and_b32_e32 v204, 0xffff0000, v204
	s_add_u32 s56, s56, 0x8000
	v_or_b32_sdwa v205, v205, v201 dst_sel:DWORD dst_unused:UNUSED_PAD src0_sel:DWORD src1_sel:WORD_1
	v_or_b32_sdwa v204, v204, v200 dst_sel:DWORD dst_unused:UNUSED_PAD src0_sel:DWORD src1_sel:WORD_1
	s_addc_u32 s57, s57, 0
	global_store_dwordx2 v[202:203], v[204:205], off offset:3104
	v_add_u32_e32 v29, 0x200, v29
	s_waitcnt vmcnt(14)
	v_add_u32_e32 v28, -16, v29
	ds_read_b128 v[30:33], v28
	ds_read_b128 v[34:37], v29
	s_mov_b32 s58, 0x800000
	s_waitcnt lgkmcnt(1)
	v_mov_b32_e32 v38, v31
	v_mov_b32_e32 v39, v32
	v_mov_b32_e32 v31, v33
	v_pk_add_f32 v[30:31], v[38:39], v[30:31]
	s_waitcnt lgkmcnt(0)
	v_mov_b32_e32 v32, v36
	v_mov_b32_e32 v33, v34
	v_mov_b32_e32 v34, v37
	v_pk_add_f32 v[32:33], v[32:33], v[34:35]
	v_add_f32_e32 v28, v30, v31
	v_add_f32_e32 v28, v28, v33
	v_add_f32_e32 v28, v32, v28
	v_fmamk_f32 v28, v28, 0x3b800000, v195
	v_cmp_gt_f32_e32 vcc, s58, v28
	v_mul_f32_e32 v30, 0x4b800000, v28
	v_lshlrev_b32_e32 v33, 16, v211
	v_cndmask_b32_e32 v28, v28, v30, vcc
	v_rsq_f32_e32 v28, v28
	v_lshlrev_b32_e32 v32, 16, v210
	v_and_b32_e32 v211, 0xffff0000, v211
	v_and_b32_e32 v210, 0xffff0000, v210
	v_mul_f32_e32 v30, 0x45800000, v28
	v_cndmask_b32_e32 v28, v28, v30, vcc
	v_pk_mul_f32 v[32:33], v[28:29], v[32:33] op_sel_hi:[0,1]
	v_pk_mul_f32 v[32:33], v[0:1], v[32:33]
	v_lshlrev_b32_e32 v35, 16, v209
	v_lshlrev_b32_e32 v34, 16, v208
	v_pk_mul_f32 v[210:211], v[28:29], v[210:211] op_sel_hi:[0,1]
	v_pk_mul_f32 v[32:33], v[32:33], v[34:35]
	v_pk_mul_f32 v[210:211], v[8:9], v[210:211]
	v_and_b32_e32 v209, 0xffff0000, v209
	v_and_b32_e32 v208, 0xffff0000, v208
	v_pk_mul_f32 v[208:209], v[210:211], v[208:209]
	v_and_b32_sdwa v211, v32, v198 dst_sel:DWORD dst_unused:UNUSED_PAD src0_sel:WORD_1 src1_sel:DWORD
	v_and_b32_sdwa v210, v33, v198 dst_sel:DWORD dst_unused:UNUSED_PAD src0_sel:WORD_1 src1_sel:DWORD
	v_add3_u32 v211, v32, v211, s71
	v_and_b32_sdwa v32, v209, v198 dst_sel:DWORD dst_unused:UNUSED_PAD src0_sel:WORD_1 src1_sel:DWORD
	v_add3_u32 v210, v33, v210, s71
	v_and_b32_sdwa v33, v208, v198 dst_sel:DWORD dst_unused:UNUSED_PAD src0_sel:WORD_1 src1_sel:DWORD
	v_add3_u32 v209, v209, v32, s71
	v_lshl_add_u64 v[30:31], v[10:11], 0, s[56:57]
	v_add3_u32 v208, v208, v33, s71
	v_and_b32_e32 v209, 0xffff0000, v209
	v_and_b32_e32 v208, 0xffff0000, v208
	v_or_b32_sdwa v209, v209, v210 dst_sel:DWORD dst_unused:UNUSED_PAD src0_sel:DWORD src1_sel:WORD_1
	v_add_co_u32_e32 v210, vcc, s72, v30
	v_or_b32_sdwa v208, v208, v211 dst_sel:DWORD dst_unused:UNUSED_PAD src0_sel:DWORD src1_sel:WORD_1
	s_nop 0
	v_addc_co_u32_e32 v211, vcc, 0, v31, vcc
	global_store_dwordx2 v[210:211], v[208:209], off offset:3072
	v_lshlrev_b32_e32 v209, 16, v215
	v_lshlrev_b32_e32 v208, 16, v214
	v_pk_mul_f32 v[208:209], v[28:29], v[208:209] op_sel_hi:[0,1]
	v_and_b32_e32 v215, 0xffff0000, v215
	v_and_b32_e32 v214, 0xffff0000, v214
	v_pk_mul_f32 v[208:209], v[4:5], v[208:209]
	v_lshlrev_b32_e32 v31, 16, v213
	v_lshlrev_b32_e32 v30, 16, v212
	v_pk_mul_f32 v[214:215], v[28:29], v[214:215] op_sel_hi:[0,1]
	v_pk_mul_f32 v[208:209], v[208:209], v[30:31]
	v_pk_mul_f32 v[214:215], v[2:3], v[214:215]
	v_and_b32_e32 v213, 0xffff0000, v213
	v_and_b32_e32 v212, 0xffff0000, v212
	v_pk_mul_f32 v[212:213], v[214:215], v[212:213]
	v_and_b32_sdwa v214, v209, v198 dst_sel:DWORD dst_unused:UNUSED_PAD src0_sel:WORD_1 src1_sel:DWORD
	v_and_b32_sdwa v215, v208, v198 dst_sel:DWORD dst_unused:UNUSED_PAD src0_sel:WORD_1 src1_sel:DWORD
	v_add3_u32 v208, v208, v215, s71
	v_add3_u32 v209, v209, v214, s71
	v_and_b32_sdwa v214, v213, v198 dst_sel:DWORD dst_unused:UNUSED_PAD src0_sel:WORD_1 src1_sel:DWORD
	v_and_b32_sdwa v215, v212, v198 dst_sel:DWORD dst_unused:UNUSED_PAD src0_sel:WORD_1 src1_sel:DWORD
	v_add3_u32 v213, v213, v214, s71
	v_add3_u32 v212, v212, v215, s71
	v_and_b32_e32 v213, 0xffff0000, v213
	v_and_b32_e32 v212, 0xffff0000, v212
	s_add_u32 s56, s56, 0x8000
	v_or_b32_sdwa v213, v213, v209 dst_sel:DWORD dst_unused:UNUSED_PAD src0_sel:DWORD src1_sel:WORD_1
	v_or_b32_sdwa v212, v212, v208 dst_sel:DWORD dst_unused:UNUSED_PAD src0_sel:DWORD src1_sel:WORD_1
	s_addc_u32 s57, s57, 0
	global_store_dwordx2 v[210:211], v[212:213], off offset:3104
	v_add_u32_e32 v29, 0x200, v29
	v_readlane_b32 s49, v253, 63
	s_add_i32 s52, s52, s49
	s_add_i32 s63, s63, s64
	s_cmpk_lt_i32 s52, 0x200
	s_barrier
	s_cbranch_scc1 .LBB0_759
	v_readlane_b32 s64, v253, 45
	v_readlane_b32 s48, v252, 16
	v_readlane_b32 s2, v252, 14
	v_readlane_b32 s68, v253, 49
	v_readlane_b32 s69, v253, 50
	v_readlane_b32 s72, v253, 53
	v_readlane_b32 s73, v253, 54
	v_readlane_b32 s84, v253, 63
	v_readlane_b32 s85, v252, 0
	v_readlane_b32 s86, v252, 1
	v_readlane_b32 s87, v252, 2
	v_readlane_b32 s90, v252, 3
	v_readlane_b32 s49, v252, 17
	v_readlane_b32 s3, v252, 15
	v_readlane_b32 s65, v253, 46
	v_readlane_b32 s66, v253, 47
	v_readlane_b32 s67, v253, 48
	v_readlane_b32 s70, v253, 51
	v_readlane_b32 s71, v253, 52
	v_readlane_b32 s74, v253, 55
	v_readlane_b32 s75, v253, 56
	v_readlane_b32 s76, v253, 57
	v_readlane_b32 s77, v253, 58
	v_readlane_b32 s78, v253, 59
	v_readlane_b32 s79, v253, 60
